# cache policy: nt on the once-read streaming row loads of the final phase loop and both p9 scatter loops (48 loads)
# speedup vs baseline: 1.0057x; 1.0016x over previous
.LBB0_1847:
	v_mov_b32_e32 v5, s20
	ds_read_b96 v[40:42], v5
	s_waitcnt lgkmcnt(0)
	v_readfirstlane_b32 s2, v40
	s_ashr_i32 s3, s2, 31
	s_lshl_b64 s[22:23], s[2:3], 2
	s_add_u32 s22, s9, s22
	s_addc_u32 s23, s10, s23
	s_lshl_b64 s[2:3], s[2:3], 12
	v_lshl_add_u64 v[22:23], v[16:17], 0, s[2:3]
	v_ashrrev_i32_e32 v35, 31, v41
	v_mov_b32_e32 v34, v41
	v_ashrrev_i32_e32 v41, 31, v42
	v_mov_b32_e32 v40, v42
	global_load_dword v20, v4, s[22:23] nt
	global_load_dwordx2 v[30:31], v[22:23], off nt
	global_load_dwordx2 v[44:45], v[22:23], off offset:512 nt
	global_load_dwordx2 v[36:37], v[22:23], off offset:1024 nt
	global_load_dwordx2 v[32:33], v[22:23], off offset:1536 nt
	global_load_dwordx2 v[28:29], v[22:23], off offset:2048 nt
	global_load_dwordx2 v[26:27], v[22:23], off offset:2560 nt
	global_load_dwordx2 v[24:25], v[22:23], off offset:3072 nt
	s_nop 0
	global_load_dwordx2 v[22:23], v[22:23], off offset:3584 nt
	v_lshlrev_b64 v[46:47], 12, v[40:41]
	v_mov_b64_e32 v[40:41], v[166:167]
	v_mov_b64_e32 v[42:43], v[168:169]
	v_lshlrev_b64 v[34:35], 12, v[34:35]
	s_add_i32 s21, s21, 8
	s_addk_i32 s20, 0x80
	s_cmp_gt_i32 s21, 55
	s_waitcnt vmcnt(7)
	v_lshlrev_b32_e32 v48, 16, v30
	v_and_b32_e32 v49, 0xffff0000, v30
	v_lshlrev_b32_e32 v30, 16, v31
	v_and_b32_e32 v31, 0xffff0000, v31
	s_waitcnt vmcnt(0)
	v_pk_mul_f32 v[40:41], v[40:41], v[48:49]
	v_pk_mul_f32 v[30:31], v[42:43], v[30:31]
	v_pk_mul_f32 v[40:41], v[20:21], v[40:41] op_sel_hi:[0,1]
	v_pk_mul_f32 v[30:31], v[20:21], v[30:31] op_sel_hi:[0,1]
	v_cvt_pk_bf16_f32 v40, v40, v41
	v_cvt_pk_bf16_f32 v41, v30, v31
	v_lshl_add_u64 v[30:31], v[18:19], 0, v[34:35]
	v_lshl_add_u64 v[34:35], v[18:19], 0, v[46:47]
	global_store_dwordx2 v[30:31], v[40:41], off
	global_store_dwordx2 v[34:35], v[40:41], off
	v_mov_b64_e32 v[40:41], v[170:171]
	v_mov_b64_e32 v[42:43], v[172:173]
	v_lshlrev_b32_e32 v46, 16, v44
	v_and_b32_e32 v47, 0xffff0000, v44
	v_lshlrev_b32_e32 v44, 16, v45
	v_and_b32_e32 v45, 0xffff0000, v45
	v_pk_mul_f32 v[40:41], v[40:41], v[46:47]
	v_pk_mul_f32 v[42:43], v[42:43], v[44:45]
	v_pk_mul_f32 v[40:41], v[20:21], v[40:41] op_sel_hi:[0,1]
	v_pk_mul_f32 v[42:43], v[20:21], v[42:43] op_sel_hi:[0,1]
	v_cvt_pk_bf16_f32 v40, v40, v41
	v_cvt_pk_bf16_f32 v41, v42, v43
	global_store_dwordx2 v[30:31], v[40:41], off offset:512
	global_store_dwordx2 v[34:35], v[40:41], off offset:512
	v_mov_b64_e32 v[40:41], v[174:175]
	v_mov_b64_e32 v[42:43], v[176:177]
	v_lshlrev_b32_e32 v44, 16, v36
	v_and_b32_e32 v45, 0xffff0000, v36
	v_pk_mul_f32 v[40:41], v[40:41], v[44:45]
	s_nop 0
	v_pk_mul_f32 v[40:41], v[20:21], v[40:41] op_sel_hi:[0,1]
	v_cvt_pk_bf16_f32 v36, v40, v41
	v_lshlrev_b32_e32 v40, 16, v37
	v_and_b32_e32 v41, 0xffff0000, v37
	v_pk_mul_f32 v[40:41], v[42:43], v[40:41]
	s_nop 0
	v_pk_mul_f32 v[40:41], v[20:21], v[40:41] op_sel_hi:[0,1]
	v_cvt_pk_bf16_f32 v37, v40, v41
	global_store_dwordx2 v[30:31], v[36:37], off offset:1024
	global_store_dwordx2 v[34:35], v[36:37], off offset:1024
	v_mov_b64_e32 v[40:41], v[178:179]
	v_mov_b64_e32 v[42:43], v[180:181]
	v_lshlrev_b32_e32 v36, 16, v32
	v_and_b32_e32 v37, 0xffff0000, v32
	v_pk_mul_f32 v[36:37], v[40:41], v[36:37]
	s_nop 0
	v_pk_mul_f32 v[36:37], v[20:21], v[36:37] op_sel_hi:[0,1]
	v_cvt_pk_bf16_f32 v32, v36, v37
	v_lshlrev_b32_e32 v36, 16, v33
	v_and_b32_e32 v37, 0xffff0000, v33
	v_pk_mul_f32 v[36:37], v[42:43], v[36:37]
	s_nop 0
	v_pk_mul_f32 v[36:37], v[20:21], v[36:37] op_sel_hi:[0,1]
	v_cvt_pk_bf16_f32 v33, v36, v37
	global_store_dwordx2 v[30:31], v[32:33], off offset:1536
	global_store_dwordx2 v[34:35], v[32:33], off offset:1536
	v_mov_b64_e32 v[40:41], v[182:183]
	v_mov_b64_e32 v[42:43], v[184:185]
	v_lshlrev_b32_e32 v32, 16, v28
	v_and_b32_e32 v33, 0xffff0000, v28
	v_pk_mul_f32 v[32:33], v[40:41], v[32:33]
	s_nop 0
	v_pk_mul_f32 v[32:33], v[20:21], v[32:33] op_sel_hi:[0,1]
	v_cvt_pk_bf16_f32 v28, v32, v33
	v_lshlrev_b32_e32 v32, 16, v29
	v_and_b32_e32 v33, 0xffff0000, v29
	v_pk_mul_f32 v[32:33], v[42:43], v[32:33]
	s_nop 0
	v_pk_mul_f32 v[32:33], v[20:21], v[32:33] op_sel_hi:[0,1]
	v_cvt_pk_bf16_f32 v29, v32, v33
	global_store_dwordx2 v[30:31], v[28:29], off offset:2048
	global_store_dwordx2 v[34:35], v[28:29], off offset:2048
	v_mov_b64_e32 v[40:41], v[186:187]
	v_mov_b64_e32 v[42:43], v[188:189]
	v_lshlrev_b32_e32 v28, 16, v26
	v_and_b32_e32 v29, 0xffff0000, v26
	v_lshlrev_b32_e32 v32, 16, v24
	v_and_b32_e32 v33, 0xffff0000, v24
	v_pk_mul_f32 v[28:29], v[40:41], v[28:29]
	s_nop 0
	v_pk_mul_f32 v[28:29], v[20:21], v[28:29] op_sel_hi:[0,1]
	v_cvt_pk_bf16_f32 v26, v28, v29
	v_lshlrev_b32_e32 v28, 16, v27
	v_and_b32_e32 v29, 0xffff0000, v27
	v_pk_mul_f32 v[28:29], v[42:43], v[28:29]
	s_nop 0
	v_pk_mul_f32 v[28:29], v[20:21], v[28:29] op_sel_hi:[0,1]
	v_cvt_pk_bf16_f32 v27, v28, v29
	global_store_dwordx2 v[30:31], v[26:27], off offset:2560
	global_store_dwordx2 v[34:35], v[26:27], off offset:2560
	v_mov_b64_e32 v[26:27], v[190:191]
	v_mov_b64_e32 v[28:29], v[192:193]
	v_pk_mul_f32 v[26:27], v[26:27], v[32:33]
	s_nop 0
	v_pk_mul_f32 v[26:27], v[20:21], v[26:27] op_sel_hi:[0,1]
	v_cvt_pk_bf16_f32 v24, v26, v27
	v_lshlrev_b32_e32 v26, 16, v25
	v_and_b32_e32 v27, 0xffff0000, v25
	v_pk_mul_f32 v[26:27], v[28:29], v[26:27]
	v_lshlrev_b32_e32 v28, 16, v22
	v_pk_mul_f32 v[26:27], v[20:21], v[26:27] op_sel_hi:[0,1]
	v_cvt_pk_bf16_f32 v25, v26, v27
	global_store_dwordx2 v[30:31], v[24:25], off offset:3072
	global_store_dwordx2 v[34:35], v[24:25], off offset:3072
	v_mov_b64_e32 v[24:25], v[194:195]
	v_mov_b64_e32 v[26:27], v[196:197]
	v_and_b32_e32 v29, 0xffff0000, v22
	v_pk_mul_f32 v[24:25], v[24:25], v[28:29]
	s_nop 0
	v_pk_mul_f32 v[24:25], v[20:21], v[24:25] op_sel_hi:[0,1]
	v_cvt_pk_bf16_f32 v22, v24, v25
	v_lshlrev_b32_e32 v24, 16, v23
	v_and_b32_e32 v25, 0xffff0000, v23
	v_pk_mul_f32 v[24:25], v[26:27], v[24:25]
	s_nop 0
	v_pk_mul_f32 v[20:21], v[20:21], v[24:25] op_sel_hi:[0,1]
	v_cvt_pk_bf16_f32 v23, v20, v21
	global_store_dwordx2 v[30:31], v[22:23], off offset:3584
	global_store_dwordx2 v[34:35], v[22:23], off offset:3584
	s_cbranch_scc0 .LBB0_1847
	s_branch .LBB0_1800

.LBB0_4165:
	v_mov_b32_e32 v5, s16
	ds_read_b96 v[28:30], v5
	s_waitcnt lgkmcnt(0)
	v_readfirstlane_b32 s2, v28
	s_ashr_i32 s3, s2, 31
	s_lshl_b64 s[18:19], s[2:3], 2
	s_add_u32 s18, s20, s18
	s_addc_u32 s19, s21, s19
	s_lshl_b64 s[2:3], s[2:3], 12
	v_lshl_add_u64 v[20:21], v[16:17], 0, s[2:3]
	global_load_dword v28, v4, s[18:19] nt
	global_load_dwordx2 v[32:33], v[20:21], off nt
	v_mov_b64_e32 v[24:25], v[166:167]
	v_mov_b64_e32 v[26:27], v[168:169]
	v_ashrrev_i32_e32 v35, 31, v29
	v_mov_b32_e32 v34, v29
	v_ashrrev_i32_e32 v31, 31, v30
	v_lshlrev_b64 v[34:35], 12, v[34:35]
	v_lshlrev_b64 v[30:31], 12, v[30:31]
	v_lshl_add_u64 v[34:35], v[18:19], 0, v[34:35]
	v_lshl_add_u64 v[30:31], v[18:19], 0, v[30:31]
	global_load_dwordx2 v[36:37], v[20:21], off offset:512 nt
	global_load_dwordx2 v[38:39], v[20:21], off offset:1024 nt
	global_load_dwordx2 v[40:41], v[20:21], off offset:1536 nt
	global_load_dwordx2 v[42:43], v[20:21], off offset:2048 nt
	global_load_dwordx2 v[44:45], v[20:21], off offset:2560 nt
	global_load_dwordx2 v[46:47], v[20:21], off offset:3072 nt
	s_nop 0
	global_load_dwordx2 v[20:21], v[20:21], off offset:3584 nt
	s_add_i32 s17, s17, 8
	s_addk_i32 s16, 0x80
	s_cmp_gt_i32 s17, 55
	s_waitcnt vmcnt(7)
	v_lshlrev_b32_e32 v48, 16, v32
	v_and_b32_e32 v49, 0xffff0000, v32
	v_lshlrev_b32_e32 v32, 16, v33
	v_and_b32_e32 v33, 0xffff0000, v33
	s_waitcnt vmcnt(7)
	v_pk_mul_f32 v[24:25], v[24:25], v[48:49]
	v_pk_mul_f32 v[26:27], v[26:27], v[32:33]
	v_pk_mul_f32 v[24:25], v[28:29], v[24:25] op_sel_hi:[0,1]
	v_pk_mul_f32 v[26:27], v[28:29], v[26:27] op_sel_hi:[0,1]
	v_cvt_pk_bf16_f32 v24, v24, v25
	v_cvt_pk_bf16_f32 v25, v26, v27
	global_store_dwordx2 v[34:35], v[24:25], off
	global_store_dwordx2 v[30:31], v[24:25], off
	v_mov_b64_e32 v[24:25], v[170:171]
	v_mov_b64_e32 v[26:27], v[172:173]
	s_waitcnt vmcnt(8)
	v_lshlrev_b32_e32 v32, 16, v36
	v_and_b32_e32 v33, 0xffff0000, v36
	v_lshlrev_b32_e32 v36, 16, v37
	v_and_b32_e32 v37, 0xffff0000, v37
	s_waitcnt vmcnt(0)
	v_pk_mul_f32 v[24:25], v[24:25], v[32:33]
	v_pk_mul_f32 v[26:27], v[26:27], v[36:37]
	v_pk_mul_f32 v[24:25], v[28:29], v[24:25] op_sel_hi:[0,1]
	v_pk_mul_f32 v[26:27], v[28:29], v[26:27] op_sel_hi:[0,1]
	v_cvt_pk_bf16_f32 v24, v24, v25
	v_cvt_pk_bf16_f32 v25, v26, v27
	global_store_dwordx2 v[34:35], v[24:25], off offset:512
	global_store_dwordx2 v[30:31], v[24:25], off offset:512
	v_mov_b64_e32 v[24:25], v[174:175]
	v_mov_b64_e32 v[26:27], v[176:177]
	v_lshlrev_b32_e32 v32, 16, v38
	v_and_b32_e32 v33, 0xffff0000, v38
	v_lshlrev_b32_e32 v36, 16, v39
	v_and_b32_e32 v37, 0xffff0000, v39
	v_pk_mul_f32 v[24:25], v[24:25], v[32:33]
	v_pk_mul_f32 v[26:27], v[26:27], v[36:37]
	v_pk_mul_f32 v[24:25], v[28:29], v[24:25] op_sel_hi:[0,1]
	v_pk_mul_f32 v[26:27], v[28:29], v[26:27] op_sel_hi:[0,1]
	v_cvt_pk_bf16_f32 v24, v24, v25
	v_cvt_pk_bf16_f32 v25, v26, v27
	global_store_dwordx2 v[34:35], v[24:25], off offset:1024
	global_store_dwordx2 v[30:31], v[24:25], off offset:1024
	v_mov_b64_e32 v[24:25], v[178:179]
	v_mov_b64_e32 v[26:27], v[180:181]
	v_lshlrev_b32_e32 v32, 16, v40
	v_and_b32_e32 v33, 0xffff0000, v40
	v_lshlrev_b32_e32 v36, 16, v41
	v_and_b32_e32 v37, 0xffff0000, v41
	v_pk_mul_f32 v[24:25], v[24:25], v[32:33]
	v_pk_mul_f32 v[26:27], v[26:27], v[36:37]
	v_pk_mul_f32 v[24:25], v[28:29], v[24:25] op_sel_hi:[0,1]
	v_pk_mul_f32 v[26:27], v[28:29], v[26:27] op_sel_hi:[0,1]
	v_cvt_pk_bf16_f32 v24, v24, v25
	v_cvt_pk_bf16_f32 v25, v26, v27
	global_store_dwordx2 v[34:35], v[24:25], off offset:1536
	global_store_dwordx2 v[30:31], v[24:25], off offset:1536
	v_mov_b64_e32 v[24:25], v[182:183]
	v_mov_b64_e32 v[26:27], v[184:185]
	v_lshlrev_b32_e32 v32, 16, v42
	v_and_b32_e32 v33, 0xffff0000, v42
	v_lshlrev_b32_e32 v36, 16, v43
	v_and_b32_e32 v37, 0xffff0000, v43
	v_pk_mul_f32 v[24:25], v[24:25], v[32:33]
	v_pk_mul_f32 v[26:27], v[26:27], v[36:37]
	v_pk_mul_f32 v[24:25], v[28:29], v[24:25] op_sel_hi:[0,1]
	v_pk_mul_f32 v[26:27], v[28:29], v[26:27] op_sel_hi:[0,1]
	v_cvt_pk_bf16_f32 v24, v24, v25
	v_cvt_pk_bf16_f32 v25, v26, v27
	global_store_dwordx2 v[34:35], v[24:25], off offset:2048
	global_store_dwordx2 v[30:31], v[24:25], off offset:2048
	v_mov_b64_e32 v[24:25], v[186:187]
	v_mov_b64_e32 v[26:27], v[188:189]
	v_lshlrev_b32_e32 v32, 16, v44
	v_and_b32_e32 v33, 0xffff0000, v44
	v_lshlrev_b32_e32 v36, 16, v45
	v_and_b32_e32 v37, 0xffff0000, v45
	v_pk_mul_f32 v[24:25], v[24:25], v[32:33]
	v_pk_mul_f32 v[26:27], v[26:27], v[36:37]
	v_pk_mul_f32 v[24:25], v[28:29], v[24:25] op_sel_hi:[0,1]
	v_pk_mul_f32 v[26:27], v[28:29], v[26:27] op_sel_hi:[0,1]
	v_cvt_pk_bf16_f32 v24, v24, v25
	v_cvt_pk_bf16_f32 v25, v26, v27
	global_store_dwordx2 v[34:35], v[24:25], off offset:2560
	global_store_dwordx2 v[30:31], v[24:25], off offset:2560
	v_mov_b64_e32 v[24:25], v[190:191]
	v_mov_b64_e32 v[26:27], v[192:193]
	v_lshlrev_b32_e32 v32, 16, v46
	v_and_b32_e32 v33, 0xffff0000, v46
	v_lshlrev_b32_e32 v36, 16, v47
	v_and_b32_e32 v37, 0xffff0000, v47
	v_pk_mul_f32 v[24:25], v[24:25], v[32:33]
	v_pk_mul_f32 v[26:27], v[26:27], v[36:37]
	v_pk_mul_f32 v[24:25], v[28:29], v[24:25] op_sel_hi:[0,1]
	v_pk_mul_f32 v[26:27], v[28:29], v[26:27] op_sel_hi:[0,1]
	v_cvt_pk_bf16_f32 v24, v24, v25
	v_cvt_pk_bf16_f32 v25, v26, v27
	global_store_dwordx2 v[34:35], v[24:25], off offset:3072
	global_store_dwordx2 v[30:31], v[24:25], off offset:3072
	v_mov_b64_e32 v[24:25], v[194:195]
	v_mov_b64_e32 v[26:27], v[196:197]
	v_lshlrev_b32_e32 v32, 16, v20
	v_and_b32_e32 v33, 0xffff0000, v20
	v_lshlrev_b32_e32 v20, 16, v21
	v_and_b32_e32 v21, 0xffff0000, v21
	v_pk_mul_f32 v[24:25], v[24:25], v[32:33]
	v_pk_mul_f32 v[20:21], v[26:27], v[20:21]
	v_pk_mul_f32 v[24:25], v[28:29], v[24:25] op_sel_hi:[0,1]
	v_pk_mul_f32 v[20:21], v[28:29], v[20:21] op_sel_hi:[0,1]
	v_cvt_pk_bf16_f32 v24, v24, v25
	v_cvt_pk_bf16_f32 v25, v20, v21
	global_store_dwordx2 v[34:35], v[24:25], off offset:3584
	global_store_dwordx2 v[30:31], v[24:25], off offset:3584
	s_cbranch_scc0 .LBB0_4165
	s_branch .LBB0_4118

.LBB0_4626:
	s_or_b64 exec, exec, s[0:1]
	s_ashr_i32 s0, s3, 6
	s_add_i32 s4, s0, s78
	s_cmpk_gt_i32 s4, 0x3fff
	s_waitcnt lgkmcnt(0)
	s_barrier
	s_cbranch_scc1 .LBB0_4629
	v_and_b32_e32 v2, 63, v0
	v_lshlrev_b32_e32 v4, 4, v2
	v_lshlrev_b32_e32 v0, 2, v2
	v_mov_b32_e32 v5, 0
	v_xor_b32_e32 v56, 64, v0
	v_xor_b32_e32 v57, 0x80, v0
	v_or_b32_e32 v0, 0x1000, v4
	v_mov_b32_e32 v1, v5
	v_lshl_add_u64 v[8:9], s[70:71], 0, v[0:1]
	v_or_b32_e32 v0, 0x1400, v4
	s_add_u32 s10, s74, 0x3b400000
	v_lshl_add_u64 v[10:11], s[70:71], 0, v[0:1]
	v_or_b32_e32 v0, 0x1800, v4
	s_addc_u32 s11, s75, 0
	v_lshl_add_u64 v[12:13], s[70:71], 0, v[0:1]
	v_or_b32_e32 v0, 0x1c00, v4
	s_add_u32 s12, s74, 0x3b500000
	v_lshl_add_u64 v[14:15], s[70:71], 0, v[0:1]
	v_lshlrev_b32_e32 v0, 3, v2
	s_addc_u32 s13, s75, 0
	v_lshl_add_u64 v[2:3], s[74:75], 0, v[0:1]
	s_mov_b64 s[2:3], 0x26c00000
	s_lshl_b32 s1, s96, 4
	s_lshl_b32 s0, s0, 1
	s_ashr_i32 s5, s4, 31
	v_lshl_add_u64 v[16:17], v[2:3], 0, s[2:3]
	s_add_i32 s2, s1, s0
	s_lshl_b32 s14, s76, 4
	s_lshl_b64 s[0:1], s[4:5], 12
	s_add_u32 s0, s74, s0
	s_addc_u32 s1, s75, s1
	v_lshl_add_u64 v[0:1], s[0:1], 0, v[0:1]
	s_mov_b64 s[0:1], 0xe400000
	s_ashr_i32 s95, s94, 31
	v_lshl_add_u64 v[18:19], v[0:1], 0, s[0:1]
	s_lshl_b64 s[6:7], s[94:95], 12
	s_lshl_b64 s[0:1], s[4:5], 13
	s_add_u32 s0, s72, s0
	s_addc_u32 s1, s73, s1
	v_lshl_add_u64 v[0:1], s[0:1], 0, v[4:5]
	s_mov_b64 s[0:1], 0x1000
	v_lshl_add_u64 v[6:7], s[70:71], 0, v[4:5]
	v_lshl_add_u64 v[20:21], v[0:1], 0, s[0:1]
	s_lshl_b64 s[8:9], s[94:95], 13
	s_add_i32 s5, 0, 0x20080
	v_mov_b32_e32 v4, 0x358637bd
	s_mov_b32 s15, 0xf800000
	v_mov_b32_e32 v58, 0x260
	global_load_dwordx4 v[130:133], v[6:7], off
	global_load_dwordx4 v[134:137], v[6:7], off offset:1024
	global_load_dwordx4 v[138:141], v[6:7], off offset:2048
	global_load_dwordx4 v[142:145], v[6:7], off offset:3072
	global_load_dwordx4 v[146:149], v[8:9], off
	global_load_dwordx4 v[150:153], v[10:11], off
	global_load_dwordx4 v[154:157], v[12:13], off
	global_load_dwordx4 v[158:161], v[14:15], off
	s_waitcnt vmcnt(0)
	s_ashr_i32 s3, s2, 31
	s_lshl_b64 s[0:1], s[2:3], 2
	s_add_u32 s16, s10, s0
	s_addc_u32 s17, s11, s1
	global_load_dwordx2 v[162:163], v[18:19], off offset:2560
	global_load_dwordx2 v[164:165], v[18:19], off offset:3072
	global_load_dwordx2 v[166:167], v[18:19], off offset:3584
	global_load_dwordx2 v[168:169], v[18:19], off offset:1024
	global_load_dwordx2 v[170:171], v[18:19], off offset:1536
	global_load_dwordx2 v[172:173], v[18:19], off offset:2048
	global_load_dwordx2 v[174:175], v[18:19], off
	global_load_dwordx2 v[176:177], v[18:19], off offset:512
	global_load_dwordx2 v[178:179], v5, s[16:17] nt
	s_add_i32 s18, s2, 1
	s_ashr_i32 s19, s18, 31
	s_add_u32 s0, s12, s0
	s_addc_u32 s1, s13, s1
	global_load_dword v180, v5, s[0:1] nt
	s_lshl_b64 s[16:17], s[18:19], 2
	s_add_u32 s0, s12, s16
	s_addc_u32 s1, s13, s17
	global_load_dword v181, v5, s[0:1] nt
	s_add_i32 s4, s4, s94
	s_add_i32 s2, s2, s14
	v_lshl_add_u64 v[18:19], v[18:19], 0, s[6:7]
	s_waitcnt vmcnt(0)
.LBB0_4628:
	v_mov_b64_e32 v[22:23], v[162:163]
	v_mov_b64_e32 v[24:25], v[164:165]
	v_mov_b64_e32 v[30:31], v[166:167]
	v_mov_b64_e32 v[42:43], v[168:169]
	v_mov_b64_e32 v[46:47], v[170:171]
	v_mov_b64_e32 v[26:27], v[172:173]
	v_mov_b64_e32 v[52:53], v[174:175]
	v_mov_b64_e32 v[34:35], v[176:177]
	v_mov_b64_e32 v[60:61], v[178:179]
	v_mov_b64_e32 v[28:29], v[180:181]
	s_ashr_i32 s3, s2, 31
	s_lshl_b64 s[0:1], s[2:3], 2
	s_add_u32 s16, s10, s0
	s_addc_u32 s17, s11, s1
	global_load_dwordx2 v[162:163], v[18:19], off offset:2560 nt
	global_load_dwordx2 v[164:165], v[18:19], off offset:3072 nt
	global_load_dwordx2 v[166:167], v[18:19], off offset:3584 nt
	global_load_dwordx2 v[168:169], v[18:19], off offset:1024 nt
	global_load_dwordx2 v[170:171], v[18:19], off offset:1536 nt
	global_load_dwordx2 v[172:173], v[18:19], off offset:2048 nt
	global_load_dwordx2 v[174:175], v[18:19], off nt
	global_load_dwordx2 v[176:177], v[18:19], off offset:512 nt
	global_load_dwordx2 v[178:179], v5, s[16:17] nt
	s_add_i32 s18, s2, 1
	s_ashr_i32 s19, s18, 31
	s_add_u32 s0, s12, s0
	s_addc_u32 s1, s13, s1
	global_load_dword v180, v5, s[0:1] nt
	s_lshl_b64 s[16:17], s[18:19], 2
	s_add_u32 s0, s12, s16
	s_addc_u32 s1, s13, s17
	global_load_dword v181, v5, s[0:1] nt
	s_add_i32 s4, s4, s94
	s_add_i32 s2, s2, s14
	v_lshl_add_u64 v[18:19], v[18:19], 0, s[6:7]
	s_sub_i32 s3, s4, s94
	s_cmpk_lt_i32 s3, 0x4000
	v_and_b32_e32 v59, 0xffff0000, v22
	v_lshlrev_b32_e32 v36, 16, v24
	v_and_b32_e32 v114, 0xffff0000, v24
	v_lshlrev_b32_e32 v38, 16, v25
	v_and_b32_e32 v126, 0xffff0000, v25
	v_lshlrev_b32_e32 v48, 16, v27
	v_and_b32_e32 v49, 0xffff0000, v27
	v_lshlrev_b32_e32 v62, 16, v26
	v_and_b32_e32 v63, 0xffff0000, v26
	v_lshlrev_b32_e32 v26, 16, v23
	v_and_b32_e32 v27, 0xffff0000, v23
	v_lshrrev_b32_e32 v23, 18, v60
	v_lshrrev_b32_e32 v24, 18, v61
	v_and_b32_e32 v23, 0x3ffc, v23
	v_and_b32_e32 v24, 0x3ffc, v24
	v_add_u32_e32 v23, s5, v23
	v_add_u32_e32 v24, s5, v24
	ds_read_b32 v23, v23
	ds_read_b32 v37, v24
	v_lshlrev_b32_e32 v127, 16, v30
	v_and_b32_e32 v25, 0xffff0000, v30
	v_and_b32_e32 v30, 0xfffff, v60
	v_and_b32_e32 v32, 0xfffff, v61
	s_waitcnt lgkmcnt(1)
	v_add_u32_e32 v64, v23, v30
	s_waitcnt lgkmcnt(0)
	v_add_u32_e32 v66, v37, v32
	v_ashrrev_i32_e32 v65, 31, v64
	v_ashrrev_i32_e32 v67, 31, v66
	v_lshlrev_b64 v[64:65], 12, v[64:65]
	v_lshlrev_b64 v[66:67], 12, v[66:67]
	v_lshl_add_u64 v[64:65], v[16:17], 0, v[64:65]
	v_lshl_add_u64 v[66:67], v[16:17], 0, v[66:67]
	global_load_dwordx2 v[68:69], v[66:67], off offset:512 nt
	global_load_dwordx2 v[70:71], v[64:65], off offset:512 nt
	global_load_dwordx2 v[72:73], v[66:67], off offset:2048 nt
	global_load_dwordx2 v[74:75], v[64:65], off offset:2048 nt
	global_load_dwordx2 v[76:77], v[66:67], off offset:2560 nt
	global_load_dwordx2 v[78:79], v[64:65], off offset:2560 nt
	global_load_dwordx2 v[80:81], v[66:67], off offset:3072 nt
	global_load_dwordx2 v[82:83], v[64:65], off offset:3072 nt
	global_load_dwordx2 v[84:85], v[64:65], off offset:3584 nt
	global_load_dwordx2 v[86:87], v[66:67], off offset:3584 nt
	global_load_dwordx2 v[88:89], v[64:65], off offset:1024 nt
	global_load_dwordx2 v[90:91], v[66:67], off offset:1024 nt
	global_load_dwordx2 v[92:93], v[64:65], off offset:1536 nt
	global_load_dwordx2 v[94:95], v[66:67], off offset:1536 nt
	global_load_dwordx2 v[96:97], v[64:65], off nt
	s_nop 0
	global_load_dwordx2 v[64:65], v[66:67], off nt
	v_mov_b32_e32 v24, v29
	v_lshlrev_b32_e32 v33, 16, v31
	v_and_b32_e32 v31, 0xffff0000, v31
	v_lshlrev_b32_e32 v50, 16, v52
	v_and_b32_e32 v51, 0xffff0000, v52
	v_lshlrev_b32_e32 v52, 16, v53
	v_and_b32_e32 v53, 0xffff0000, v53
	v_lshlrev_b32_e32 v54, 16, v34
	v_and_b32_e32 v55, 0xffff0000, v34
	v_lshlrev_b32_e32 v34, 16, v35
	v_and_b32_e32 v35, 0xffff0000, v35
	v_lshlrev_b32_e32 v22, 16, v22
	v_lshlrev_b32_e32 v41, 16, v43
	v_lshlrev_b32_e32 v40, 16, v42
	v_and_b32_e32 v43, 0xffff0000, v43
	v_and_b32_e32 v42, 0xffff0000, v42
	v_lshlrev_b32_e32 v45, 16, v47
	v_lshlrev_b32_e32 v44, 16, v46
	v_and_b32_e32 v47, 0xffff0000, v47
	v_and_b32_e32 v46, 0xffff0000, v46
	v_mov_b32_e32 v61, v28
	s_waitcnt vmcnt(15)
	v_lshlrev_b32_e32 v67, 16, v68
	s_waitcnt vmcnt(14)
	v_lshlrev_b32_e32 v66, 16, v70
	v_and_b32_e32 v99, 0xffff0000, v68
	v_and_b32_e32 v98, 0xffff0000, v70
	v_lshlrev_b32_e32 v101, 16, v69
	v_lshlrev_b32_e32 v100, 16, v71
	v_and_b32_e32 v69, 0xffff0000, v69
	v_and_b32_e32 v68, 0xffff0000, v71
	s_waitcnt vmcnt(13)
	v_lshlrev_b32_e32 v71, 16, v72
	s_waitcnt vmcnt(12)
	v_lshlrev_b32_e32 v70, 16, v74
	v_and_b32_e32 v103, 0xffff0000, v72
	v_and_b32_e32 v102, 0xffff0000, v74
	s_waitcnt vmcnt(10)
	v_lshlrev_b32_e32 v104, 16, v78
	v_and_b32_e32 v106, 0xffff0000, v78
	s_waitcnt vmcnt(8)
	v_lshlrev_b32_e32 v78, 16, v82
	v_and_b32_e32 v110, 0xffff0000, v82
	s_waitcnt vmcnt(6)
	v_lshlrev_b32_e32 v115, 16, v86
	v_and_b32_e32 v32, 0xffff0000, v86
	v_lshlrev_b32_e32 v39, 16, v87
	v_and_b32_e32 v82, 0xffff0000, v87
	s_waitcnt vmcnt(4)
	v_lshlrev_b32_e32 v87, 16, v91
	v_lshlrev_b32_e32 v86, 16, v90
	v_and_b32_e32 v91, 0xffff0000, v91
	v_and_b32_e32 v90, 0xffff0000, v90
	s_waitcnt vmcnt(2)
	v_lshlrev_b32_e32 v119, 16, v95
	v_lshlrev_b32_e32 v118, 16, v94
	v_and_b32_e32 v95, 0xffff0000, v95
	v_and_b32_e32 v94, 0xffff0000, v94
	v_and_b32_e32 v121, 0xffff0000, v75
	v_lshlrev_b32_e32 v120, 16, v75
	v_and_b32_e32 v75, 0xffff0000, v73
	v_lshlrev_b32_e32 v74, 16, v73
	s_waitcnt vmcnt(1)
	v_and_b32_e32 v73, 0xffff0000, v96
	v_lshlrev_b32_e32 v72, 16, v96
	v_and_b32_e32 v125, 0xffff0000, v97
	v_lshlrev_b32_e32 v124, 16, v97
	s_waitcnt vmcnt(0)
	v_and_b32_e32 v97, 0xffff0000, v65
	v_lshlrev_b32_e32 v96, 16, v65
	v_lshlrev_b32_e32 v105, 16, v76
	v_and_b32_e32 v107, 0xffff0000, v76
	v_lshlrev_b32_e32 v108, 16, v79
	v_and_b32_e32 v76, 0xffff0000, v79
	v_lshlrev_b32_e32 v79, 16, v80
	v_and_b32_e32 v111, 0xffff0000, v80
	v_lshlrev_b32_e32 v113, 16, v81
	v_lshlrev_b32_e32 v112, 16, v83
	v_and_b32_e32 v81, 0xffff0000, v81
	v_and_b32_e32 v80, 0xffff0000, v83
	v_lshlrev_b32_e32 v83, 16, v84
	v_and_b32_e32 v23, 0xffff0000, v84
	v_lshlrev_b32_e32 v37, 16, v85
	v_and_b32_e32 v60, 0xffff0000, v85
	v_lshlrev_b32_e32 v85, 16, v89
	v_lshlrev_b32_e32 v84, 16, v88
	v_and_b32_e32 v89, 0xffff0000, v89
	v_and_b32_e32 v88, 0xffff0000, v88
	v_lshlrev_b32_e32 v117, 16, v93
	v_lshlrev_b32_e32 v116, 16, v92
	v_and_b32_e32 v93, 0xffff0000, v93
	v_and_b32_e32 v92, 0xffff0000, v92
	v_and_b32_e32 v123, 0xffff0000, v64
	v_lshlrev_b32_e32 v122, 16, v64
	v_pk_mul_f32 v[64:65], v[28:29], v[66:67]
	v_pk_mul_f32 v[66:67], v[28:29], v[98:99]
	v_pk_mul_f32 v[98:99], v[28:29], v[100:101]
	v_pk_mul_f32 v[68:69], v[28:29], v[68:69]
	v_pk_mul_f32 v[86:87], v[24:25], v[86:87] op_sel_hi:[0,1]
	v_pk_mul_f32 v[90:91], v[24:25], v[90:91] op_sel_hi:[0,1]
	v_pk_mul_f32 v[94:95], v[24:25], v[94:95] op_sel_hi:[0,1]
	v_pk_mul_f32 v[96:97], v[24:25], v[96:97] op_sel_hi:[0,1]
	v_lshlrev_b32_e32 v109, 16, v77
	v_pk_mul_f32 v[100:101], v[28:29], v[102:103]
	v_pk_mul_f32 v[102:103], v[28:29], v[106:107]
	v_pk_mul_f32 v[80:81], v[28:29], v[80:81]
	v_mul_f32_e32 v30, v29, v105
	v_pk_mul_f32 v[118:119], v[24:25], v[118:119] op_sel_hi:[0,1]
	v_pk_mul_f32 v[74:75], v[24:25], v[74:75] op_sel_hi:[0,1]
	v_pk_mul_f32 v[122:123], v[24:25], v[122:123] op_sel_hi:[0,1]
	v_mul_f32_e32 v24, v29, v79
	v_pk_fma_f32 v[84:85], v[28:29], v[84:85], v[86:87] op_sel_hi:[0,1,1]
	v_pk_fma_f32 v[86:87], v[28:29], v[88:89], v[90:91] op_sel_hi:[0,1,1]
	v_pk_fma_f32 v[90:91], v[28:29], v[92:93], v[94:95] op_sel_hi:[0,1,1]
	v_pk_fma_f32 v[92:93], v[28:29], v[124:125], v[96:97] op_sel_hi:[0,1,1]
	v_mov_b32_e32 v96, v64
	v_mov_b32_e32 v97, v66
	v_mov_b32_e32 v66, v65
	v_mov_b32_e32 v64, v98
	v_mov_b32_e32 v65, v68
	v_mov_b32_e32 v68, v99
	v_and_b32_e32 v77, 0xffff0000, v77
	v_pk_mul_f32 v[70:71], v[28:29], v[70:71]
	v_pk_mul_f32 v[106:107], v[28:29], v[108:109]
	v_pk_mul_f32 v[108:109], v[28:29], v[110:111]
	v_mul_f32_e32 v110, v28, v37
	v_mul_f32_e32 v37, v29, v39
	v_mul_f32_e32 v39, v29, v82
	v_add_f32_e32 v82, v102, v103
	v_add_f32_e32 v103, v80, v81
	v_pk_fma_f32 v[80:81], v[28:29], v[104:105], v[30:31] op_sel_hi:[1,1,0]
	v_pk_fma_f32 v[72:73], v[28:29], v[72:73], v[122:123] op_sel_hi:[0,1,1]
	v_pk_fma_f32 v[78:79], v[28:29], v[78:79], v[24:25] op_sel_hi:[1,1,0]
	v_pk_add_f32 v[66:67], v[96:97], v[66:67]
	v_pk_add_f32 v[64:65], v[64:65], v[68:69]
	v_pk_mul_f32 v[76:77], v[28:29], v[76:77]
	v_mul_f32_e32 v111, v29, v32
	v_mul_f32_e32 v32, v29, v113
	v_add_f32_e32 v102, v108, v109
	v_mov_b32_e32 v98, v70
	v_mov_b32_e32 v99, v100
	v_mov_b32_e32 v100, v71
	v_mov_b32_e32 v81, v28
	v_pk_add_f32 v[50:51], v[72:73], v[50:51]
	v_pk_add_f32 v[52:53], v[92:93], v[52:53]
	v_mov_b32_e32 v79, v110
	v_pk_add_f32 v[54:55], v[66:67], v[54:55]
	v_pk_add_f32 v[34:35], v[64:65], v[34:35]
	v_mul_f32_e32 v60, v28, v60
	v_pk_fma_f32 v[88:89], v[28:29], v[116:117], v[118:119] op_sel_hi:[0,1,1]
	v_pk_fma_f32 v[74:75], v[28:29], v[120:121], v[74:75] op_sel_hi:[0,1,1]
	v_pk_fma_f32 v[94:95], v[28:29], v[112:113], v[32:33] op_sel_hi:[1,1,0]
	v_mov_b32_e32 v70, v106
	v_mov_b32_e32 v71, v76
	v_mov_b32_e32 v76, v107
	v_add_f32_e32 v102, v102, v114
	v_pk_add_f32 v[42:43], v[86:87], v[42:43]
	v_pk_add_f32 v[46:47], v[90:91], v[46:47]
	v_pk_add_f32 v[68:69], v[98:99], v[100:101]
	v_pk_add_f32 v[72:73], v[80:81], v[22:23]
	v_pk_mul_f32 v[22:23], v[80:81], v[22:23]
	v_pk_add_f32 v[36:37], v[78:79], v[36:37]
	v_mov_b32_e32 v78, v51
	v_mov_b32_e32 v80, v53
	v_mov_b32_e32 v79, v55
	v_mov_b32_e32 v81, v35
	v_add_f32_e32 v103, v103, v126
	v_pk_add_f32 v[40:41], v[84:85], v[40:41]
	v_pk_add_f32 v[44:45], v[88:89], v[44:45]
	v_pk_add_f32 v[48:49], v[74:75], v[48:49]
	v_mov_b32_e32 v95, v60
	v_pk_add_f32 v[70:71], v[70:71], v[76:77]
	v_pk_mul_f32 v[74:75], v[42:43], v[42:43]
	v_pk_mul_f32 v[76:77], v[46:47], v[46:47]
	v_mul_f32_e32 v28, v102, v102
	v_mov_b32_e32 v66, v50
	v_mov_b32_e32 v64, v52
	v_pk_add_f32 v[62:63], v[68:69], v[62:63]
	v_mov_b32_e32 v22, v72
	v_mov_b32_e32 v110, v72
	v_mov_b32_e32 v67, v54
	v_mov_b32_e32 v65, v34
	v_pk_mul_f32 v[78:79], v[78:79], v[78:79]
	v_pk_mul_f32 v[80:81], v[80:81], v[80:81]
	v_add_f32_e32 v59, v82, v59
	v_mul_f32_e32 v60, v103, v103
	v_pk_add_f32 v[38:39], v[94:95], v[38:39]
	v_pk_add_f32 v[26:27], v[70:71], v[26:27]
	v_pk_fma_f32 v[68:69], v[40:41], v[40:41], v[74:75]
	v_pk_fma_f32 v[70:71], v[44:45], v[44:45], v[76:77]
	v_pk_mul_f32 v[76:77], v[72:73], v[72:73]
	v_pk_fma_f32 v[84:85], v[36:37], v[36:37], v[28:29]
	v_mov_b32_e32 v28, v63
	v_mov_b32_e32 v114, v63
	v_pk_add_f32 v[22:23], v[22:23], v[110:111]
	v_pk_fma_f32 v[66:67], v[66:67], v[66:67], v[78:79]
	v_pk_fma_f32 v[64:65], v[64:65], v[64:65], v[80:81]
	v_mul_f32_e32 v24, v59, v59
	v_pk_fma_f32 v[86:87], v[38:39], v[38:39], v[60:61]
	v_mov_b32_e32 v60, v62
	v_mov_b32_e32 v82, v62
	v_pk_mul_f32 v[88:89], v[26:27], v[26:27]
	v_pk_add_f32 v[68:69], v[68:69], v[68:69] op_sel:[0,1] op_sel_hi:[1,0]
	v_pk_mul_f32 v[28:29], v[28:29], v[114:115]
	v_mov_b32_e32 v77, v23
	v_pk_add_f32 v[64:65], v[66:67], v[64:65]
	v_mul_f32_e32 v30, v49, v49
	v_pk_mul_f32 v[90:91], v[60:61], v[82:83]
	v_pk_fma_f32 v[60:61], v[60:61], v[82:83], v[28:29]
	v_mov_b32_e32 v69, v29
	v_mov_b32_e32 v22, v88
	v_pk_add_f32 v[28:29], v[76:77], v[24:25]
	v_mov_b32_e32 v24, v89
	v_pk_add_f32 v[64:65], v[64:65], v[64:65] op_sel:[0,1] op_sel_hi:[1,0]
	v_pk_fma_f32 v[74:75], v[48:49], v[48:49], v[30:31] op_sel_hi:[1,1,0]
	v_pk_add_f32 v[70:71], v[70:71], v[70:71] op_sel:[0,1] op_sel_hi:[1,0]
	v_pk_add_f32 v[22:23], v[22:23], v[24:25]
	v_mov_b32_e32 v65, v91
	v_mov_b32_e32 v32, v36
	v_mov_b32_e32 v30, v38
	v_mov_b32_e32 v75, v127
	v_mov_b32_e32 v71, v127
	v_pk_add_f32 v[24:25], v[28:29], v[22:23]
	v_pk_mul_f32 v[22:23], v[28:29], v[22:23]
	v_pk_add_f32 v[64:65], v[64:65], v[68:69]
	v_pk_add_f32 v[32:33], v[36:37], v[32:33]
	v_pk_add_f32 v[30:31], v[38:39], v[30:31]
	v_pk_add_f32 v[60:61], v[60:61], v[74:75]
	v_mov_b32_e32 v25, v23
	v_pk_add_f32 v[22:23], v[64:65], v[70:71]
	v_pk_mul_f32 v[92:93], v[32:33], v[32:33]
	v_pk_mul_f32 v[94:95], v[30:31], v[30:31]
	v_pk_add_f32 v[64:65], v[22:23], v[60:61]
	v_pk_mul_f32 v[60:61], v[22:23], v[60:61]
	v_mov_b32_e32 v85, v93
	v_mov_b32_e32 v87, v95
	v_mov_b32_e32 v65, v61
	v_pk_add_f32 v[66:67], v[84:85], v[86:87]
	v_pk_add_f32 v[24:25], v[64:65], v[24:25]
	v_mov_b32_e32 v73, v59
	v_pk_add_f32 v[24:25], v[24:25], v[66:67]
	v_mov_b32_e32 v37, v102
	v_add_f32_e32 v22, v24, v25
	v_mov_b32_e32 v39, v103
	s_nop 0
	v_add_f32_dpp v22, v22, v22 quad_perm:[1,0,3,2] row_mask:0xf bank_mask:0xf bound_ctrl:1
	s_nop 1
	v_add_f32_dpp v22, v22, v22 quad_perm:[2,3,0,1] row_mask:0xf bank_mask:0xf bound_ctrl:1
	s_nop 1
	v_add_f32_dpp v22, v22, v22 row_ror:4 row_mask:0xf bank_mask:0xf bound_ctrl:1
	s_nop 1
	v_add_f32_dpp v22, v22, v22 row_ror:8 row_mask:0xf bank_mask:0xf bound_ctrl:1
	ds_bpermute_b32 v24, v56, v22
	s_waitcnt lgkmcnt(0)
	v_add_f32_e32 v22, v22, v24
	ds_bpermute_b32 v24, v57, v22
	s_waitcnt lgkmcnt(0)
	v_add_f32_e32 v22, v22, v24
	v_fmamk_f32 v22, v22, 0x3a000000, v4
	v_mul_f32_e32 v24, 0x4f800000, v22
	v_cmp_gt_f32_e32 vcc, s15, v22
	s_nop 1
	v_cndmask_b32_e32 v22, v22, v24, vcc
	v_sqrt_f32_e32 v24, v22
	s_nop 0
	v_add_u32_e32 v25, -1, v24
	v_add_u32_e32 v28, 1, v24
	v_fma_f32 v30, -v25, v24, v22
	v_fma_f32 v32, -v28, v24, v22
	v_cmp_ge_f32_e64 s[0:1], 0, v30
	s_nop 1
	v_cndmask_b32_e64 v24, v24, v25, s[0:1]
	v_cmp_lt_f32_e64 s[0:1], 0, v32
	s_nop 1
	v_cndmask_b32_e64 v24, v24, v28, s[0:1]
	v_mul_f32_e32 v25, 0x37800000, v24
	v_cndmask_b32_e32 v24, v24, v25, vcc
	v_cmp_class_f32_e32 vcc, v22, v58
	s_nop 1
	v_cndmask_b32_e32 v22, v24, v22, vcc
	v_div_scale_f32 v24, s[0:1], v22, v22, 1.0
	v_rcp_f32_e32 v28, v24
	v_div_scale_f32 v25, vcc, 1.0, v22, 1.0
	v_fma_f32 v30, -v24, v28, 1.0
	v_fmac_f32_e32 v28, v30, v28
	v_mul_f32_e32 v30, v25, v28
	v_fma_f32 v32, -v24, v30, v25
	v_fmac_f32_e32 v30, v32, v28
	v_fma_f32 v24, -v24, v30, v25
	v_div_fmas_f32 v24, v24, v28, v30
	v_div_fixup_f32 v22, v24, v22, 1.0
	v_pk_mul_f32 v[24:25], v[22:23], v[50:51] op_sel_hi:[0,1]
	v_pk_mul_f32 v[50:51], v[22:23], v[52:53] op_sel_hi:[0,1]
	v_pk_mul_f32 v[2:3], v[50:51], v[132:133]
	v_pk_mul_f32 v[0:1], v[24:25], v[130:131]
	global_store_dwordx4 v[20:21], v[0:3], off offset:-4096
	s_nop 1
	v_pk_mul_f32 v[24:25], v[22:23], v[34:35] op_sel_hi:[0,1]
	v_pk_mul_f32 v[34:35], v[22:23], v[54:55] op_sel_hi:[0,1]
	v_mov_b32_e32 v30, v33
	v_mov_b32_e32 v28, v23
	v_pk_mul_f32 v[0:1], v[34:35], v[134:135]
	v_pk_mul_f32 v[2:3], v[24:25], v[136:137]
	global_store_dwordx4 v[20:21], v[0:3], off offset:-3072
	s_nop 1
	v_mov_b32_e32 v24, v40
	v_mov_b32_e32 v25, v42
	v_mov_b32_e32 v42, v41
	v_pk_mul_f32 v[24:25], v[22:23], v[24:25] op_sel_hi:[0,1]
	v_pk_mul_f32 v[34:35], v[22:23], v[42:43] op_sel_hi:[0,1]
	v_pk_mul_f32 v[0:1], v[24:25], v[138:139]
	v_pk_mul_f32 v[2:3], v[34:35], v[140:141]
	global_store_dwordx4 v[20:21], v[0:3], off offset:-2048
	s_nop 1
	v_mov_b32_e32 v24, v44
	v_mov_b32_e32 v25, v46
	v_mov_b32_e32 v46, v45
	v_pk_mul_f32 v[24:25], v[22:23], v[24:25] op_sel_hi:[0,1]
	v_pk_mul_f32 v[34:35], v[22:23], v[46:47] op_sel_hi:[0,1]
	v_pk_mul_f32 v[0:1], v[24:25], v[142:143]
	v_pk_mul_f32 v[2:3], v[34:35], v[144:145]
	global_store_dwordx4 v[20:21], v[0:3], off offset:-1024
	s_nop 1
	v_pk_mul_f32 v[24:25], v[22:23], v[48:49] op_sel_hi:[0,1]
	v_pk_mul_f32 v[34:35], v[22:23], v[62:63] op_sel_hi:[0,1]
	v_pk_mul_f32 v[0:1], v[34:35], v[146:147]
	v_pk_mul_f32 v[2:3], v[24:25], v[148:149]
	global_store_dwordx4 v[20:21], v[0:3], off
	s_nop 1
	v_pk_mul_f32 v[24:25], v[22:23], v[26:27] op_sel_hi:[0,1]
	v_pk_mul_f32 v[26:27], v[22:23], v[72:73] op_sel_hi:[0,1]
	v_pk_mul_f32 v[0:1], v[26:27], v[150:151]
	v_pk_mul_f32 v[2:3], v[24:25], v[152:153]
	global_store_dwordx4 v[20:21], v[0:3], off offset:1024
	s_nop 1
	v_pk_mul_f32 v[24:25], v[22:23], v[38:39] op_sel_hi:[0,1]
	v_pk_mul_f32 v[26:27], v[22:23], v[36:37] op_sel_hi:[0,1]
	v_pk_mul_f32 v[0:1], v[26:27], v[154:155]
	v_pk_mul_f32 v[2:3], v[24:25], v[156:157]
	global_store_dwordx4 v[20:21], v[0:3], off offset:2048
	s_nop 1
	v_pk_mul_f32 v[24:25], v[22:23], v[28:29] op_sel_hi:[0,1]
	v_pk_mul_f32 v[22:23], v[22:23], v[30:31] op_sel_hi:[0,1]
	v_pk_mul_f32 v[0:1], v[24:25], v[158:159]
	v_pk_mul_f32 v[2:3], v[22:23], v[160:161]
	global_store_dwordx4 v[20:21], v[0:3], off offset:3072
	s_nop 1
	v_lshl_add_u64 v[20:21], v[20:21], 0, s[8:9]
	s_cbranch_scc1 .LBB0_4628
